# v55 + next-phase weight prefetch into L2: waves 1-7 of every workgroup request a slice of the first K-tiles of the next GEMM phase's weight rows while they wait in the seam (proj, out, gate_up except
# baseline (speedup 1.0000x reference)
;     __device__ void init(int M, int N, int G_, int c_) { base.init(M, N, G_, c_); full = base.nwg / G_; split = (base.nwg % G_) * 2 == G_ && (G_ % 16) == 0; }
;     __device__ void init(int G_, int c_) { base.init(MTOK, DM, G_, c_); }
; #define GAS __attribute__((address_space(1)))
; __device__ __forceinline__ unsigned xb_add(unsigned* p, unsigned v) { return __hip_atomic_fetch_add(p, v, __ATOMIC_RELAXED, __HIP_MEMORY_SCOPE_AGENT); }
; #define TSTART() do { tph0 = rt(); } while (0)
; #define TSTART() do {} while (0)
; #define WSL() GAS unsigned char* wlg = (GAS unsigned char*)ws; asm volatile("" : "+s"(wlg)); unsigned char* wl = (unsigned char*)wlg; int cb = (int)blockIdx.x, vcu_ = F.vcu, wave_ = F.wave; asm volatile("" : "+s"(cb), "+s"(vcu_), "+s"(wave_))
; __device__ __forceinline__ void xcd_barrier(const XcdBarrier& b, const bool group_local = false, const bool xcc_only = false) {
;     asm volatile("s_waitcnt vmcnt(0)" ::: "memory");
;     __syncthreads();
;     if (threadIdx.x == 0) {
;         GAS unsigned* barg = (GAS unsigned*)b.bar; asm volatile("" : "+s"(barg)); unsigned* bar = (unsigned*)barg;
;         __builtin_amdgcn_s_waitcnt(0);
;         unsigned nloc = b.st[0], nx = b.st[1];
;         if (nloc == 0u) { xcd_barrier_complete(bar, b.x, nloc, nx); b.st[0] = nloc; b.st[1] = nx; }
;         const unsigned old = xb_add(&bar[XB_XSUB(b.x)], 1u);
; __global__ void __launch_bounds__(NWAVES * 64, 2) mk_fwd(Args args) {
;     ...
;         if (IN(pb + 2)) { TSTART();
;             WSL(); const bf16* WL = (const bf16*)(wl + WS_W) + (size_t)l * LAYER_W_ELEMS;
;             pg8::Gemm g{(const bf16*)(wl + WS_YA), WL + W_PAB, 2 * MTOK, 2 * DM, GW}; pg8::ProjOrder S; S.init(F.G, cb);
.LBB0_1036:
	v_readlane_b32 s0, v255, 23
	s_add_i32 s22, s0, 3
	v_readlane_b32 s0, v255, 6
	v_readlane_b32 s1, v255, 7
	s_cmp_ge_i32 s22, s1
	s_cbranch_scc1 .LBB0_1048
	s_waitcnt vmcnt(0)
	s_waitcnt vmcnt(0)
	s_barrier
	v_cmp_lt_u32_e32 vcc, 63, v0
	s_and_saveexec_b64 s[14:15], vcc
	s_cbranch_execz .Lwp_pj
	v_readlane_b32 s0, v255, 4
	v_readlane_b32 s1, v255, 5
	v_readlane_b32 s4, v255, 52
	v_readlane_b32 s5, v255, 2
	s_mul_i32 s4, s4, 0x1dc0000
	s_add_u32 s0, s0, s4
	s_addc_u32 s1, s1, 0
	s_add_u32 s0, s0, 0x1100000
	s_addc_u32 s1, s1, 0
	s_lshr_b32 s5, s5, 3
	s_mul_i32 s5, s5, 448
	v_add_u32_e32 v241, s5, v0
	v_subrev_u32_e32 v241, 64, v241
	v_lshrrev_b32_e32 v242, 2, v241
	v_cmp_gt_u32_e32 vcc, 0x800, v242
	s_and_b64 exec, exec, vcc
	s_cbranch_execz .Lwp_pj
	v_and_b32_e32 v241, 3, v241
	v_mul_u32_u24_e32 v242, 0x400, v242
	v_lshl_add_u32 v241, v241, 7, v242
	global_load_dword v240, v241, s[0:1]
.Lwp_pj:
	s_or_b64 exec, exec, s[14:15]
	s_mov_b64 s[14:15], exec
	v_readlane_b32 s0, v255, 43
	v_readlane_b32 s1, v255, 44
	s_and_b64 s[0:1], s[14:15], s[0:1]
	v_readlane_b32 s77, v255, 52
	s_mov_b64 exec, s[0:1]
	s_cbranch_execz .LBB0_1112
	v_readlane_b32 s0, v255, 10
	v_readlane_b32 s4, v255, 12
	v_readlane_b32 s1, v255, 11
	s_waitcnt vmcnt(0) expcnt(0) lgkmcnt(0)
	v_mov_b32_e32 v4, s4
	ds_read_b32 v2, v4
	ds_read_b32 v6, v4 offset:4
	s_waitcnt lgkmcnt(1)
	v_cmp_ne_u32_e32 vcc, 0, v2
	s_cbranch_vccnz .LBB0_1054
	v_readlane_b32 s4, v255, 0
	v_readlane_b32 s5, v255, 1
	s_load_dwordx2 s[8:9], s[4:5], 0x4
	v_readlane_b32 s4, v255, 47
	s_lshl_b32 s4, s4, 2
	s_add_u32 s4, s0, s4
	s_addc_u32 s5, s1, 0
	s_add_u32 s6, s0, 0x1000
	s_addc_u32 s7, s1, 0
	s_waitcnt lgkmcnt(0)
	s_mul_i32 s23, s8, s33
	s_add_u32 s8, s0, 0x1100
	s_mul_i32 s23, s23, s9
	s_addc_u32 s9, s1, 0
	s_add_u32 s10, s0, 0x1200
	s_addc_u32 s11, s1, 0
	s_add_u32 s12, s0, 0x1300
	s_addc_u32 s13, s1, 0
	s_mov_b32 s24, 1
	s_branch .LBB0_1041

;     __device__ void init(int M, int N, int G_, int c_) { base.init(M, N, G_, c_); full = base.nwg / G_; split = (base.nwg % G_) * 2 == G_ && (G_ % 16) == 0; }
;     __device__ void init(int G_, int c_) { base.init(MTOK, DM, G_, c_); }
; #define GAS __attribute__((address_space(1)))
; __device__ __forceinline__ unsigned xb_add(unsigned* p, unsigned v) { return __hip_atomic_fetch_add(p, v, __ATOMIC_RELAXED, __HIP_MEMORY_SCOPE_AGENT); }
; #define TSTART() do { tph0 = rt(); } while (0)
; #define TSTART() do {} while (0)
; #define WSL() GAS unsigned char* wlg = (GAS unsigned char*)ws; asm volatile("" : "+s"(wlg)); unsigned char* wl = (unsigned char*)wlg; int cb = (int)blockIdx.x, vcu_ = F.vcu, wave_ = F.wave; asm volatile("" : "+s"(cb), "+s"(vcu_), "+s"(wave_))
; __device__ __forceinline__ void xcd_barrier(const XcdBarrier& b, const bool group_local = false, const bool xcc_only = false) {
;     asm volatile("s_waitcnt vmcnt(0)" ::: "memory");
;     __syncthreads();
;     if (threadIdx.x == 0) {
;         GAS unsigned* barg = (GAS unsigned*)b.bar; asm volatile("" : "+s"(barg)); unsigned* bar = (unsigned*)barg;
;         __builtin_amdgcn_s_waitcnt(0);
;         unsigned nloc = b.st[0], nx = b.st[1];
;         if (nloc == 0u) { xcd_barrier_complete(bar, b.x, nloc, nx); b.st[0] = nloc; b.st[1] = nx; }
;         const unsigned old = xb_add(&bar[XB_XSUB(b.x)], 1u);
; __global__ void __launch_bounds__(NWAVES * 64, 2) mk_fwd(Args args) {
;     ...
;         if (IN(pb + 3)) { TSTART();
;             WSL(); const bf16* WL = (const bf16*)(wl + WS_W) + (size_t)l * LAYER_W_ELEMS;
;             pg8::Gemm g{(const bf16*)(wl + WS_MERGED), WL + W_OUT, MTOK, DM, DM}; pg8::StaticOrder S; S.init(MTOK, DM, F.G, cb);
.LBB0_1206:
	v_readlane_b32 s0, v255, 23
	s_add_i32 s22, s0, 4
	v_readlane_b32 s0, v255, 6
	v_readlane_b32 s1, v255, 7
	s_cmp_ge_i32 s22, s1
	s_cbranch_scc1 .LBB0_1282
	s_waitcnt vmcnt(0)
	s_waitcnt vmcnt(0) lgkmcnt(0)
	s_barrier
	v_cmp_lt_u32_e32 vcc, 63, v0
	s_and_saveexec_b64 s[14:15], vcc
	s_cbranch_execz .Lwp_op
	v_readlane_b32 s0, v255, 4
	v_readlane_b32 s1, v255, 5
	v_readlane_b32 s4, v255, 52
	v_readlane_b32 s5, v255, 2
	s_mul_i32 s4, s4, 0x1dc0000
	s_add_u32 s0, s0, s4
	s_addc_u32 s1, s1, 0
	s_add_u32 s0, s0, 0x1300000
	s_addc_u32 s1, s1, 0
	s_lshr_b32 s5, s5, 3
	s_mul_i32 s5, s5, 448
	v_add_u32_e32 v241, s5, v0
	v_subrev_u32_e32 v241, 64, v241
	v_lshrrev_b32_e32 v242, 3, v241
	v_cmp_gt_u32_e32 vcc, 0x400, v242
	s_and_b64 exec, exec, vcc
	s_cbranch_execz .Lwp_op
	v_and_b32_e32 v241, 7, v241
	v_mul_u32_u24_e32 v242, 0x800, v242
	v_lshl_add_u32 v241, v241, 7, v242
	global_load_dword v240, v241, s[0:1]
.Lwp_op:
	s_or_b64 exec, exec, s[14:15]
	s_mov_b64 s[14:15], exec
	v_readlane_b32 s0, v255, 43
	v_readlane_b32 s1, v255, 44
	s_and_b64 s[0:1], s[14:15], s[0:1]
	s_mov_b64 exec, s[0:1]
	s_cbranch_execz .LBB0_1281
	v_readlane_b32 s0, v255, 10
	v_readlane_b32 s4, v255, 12
	v_readlane_b32 s1, v255, 11
	s_waitcnt vmcnt(0) expcnt(0) lgkmcnt(0)
	v_mov_b32_e32 v4, s4
	ds_read_b32 v2, v4
	ds_read_b32 v6, v4 offset:4
	s_waitcnt lgkmcnt(1)
	v_cmp_ne_u32_e32 vcc, 0, v2
	s_cbranch_vccnz .LBB0_1223
	v_readlane_b32 s4, v255, 0
	v_readlane_b32 s5, v255, 1
	s_load_dwordx2 s[8:9], s[4:5], 0x4
	v_readlane_b32 s4, v255, 47
	s_lshl_b32 s4, s4, 2
	s_add_u32 s4, s0, s4
	s_addc_u32 s5, s1, 0
	s_add_u32 s6, s0, 0x1000
	s_addc_u32 s7, s1, 0
	s_waitcnt lgkmcnt(0)
	s_mul_i32 s23, s8, s33
	s_add_u32 s8, s0, 0x1100
	s_mul_i32 s23, s23, s9
	s_addc_u32 s9, s1, 0
	s_add_u32 s10, s0, 0x1200
	s_addc_u32 s11, s1, 0
	s_add_u32 s12, s0, 0x1300
	s_addc_u32 s13, s1, 0
	s_mov_b32 s24, 1
	s_branch .LBB0_1211

;     __device__ void init(int M, int N, int G_, int c_) { base.init(M, N, G_, c_); full = base.nwg / G_; split = (base.nwg % G_) * 2 == G_ && (G_ % 16) == 0; }
;     __device__ void init(int G_, int c_) { base.init(MTOK, DM, G_, c_); }
; #define GAS __attribute__((address_space(1)))
; __device__ __forceinline__ unsigned xb_add(unsigned* p, unsigned v) { return __hip_atomic_fetch_add(p, v, __ATOMIC_RELAXED, __HIP_MEMORY_SCOPE_AGENT); }
; #define TSTART() do { tph0 = rt(); } while (0)
; #define TSTART() do {} while (0)
; #define WSL() GAS unsigned char* wlg = (GAS unsigned char*)ws; asm volatile("" : "+s"(wlg)); unsigned char* wl = (unsigned char*)wlg; int cb = (int)blockIdx.x, vcu_ = F.vcu, wave_ = F.wave; asm volatile("" : "+s"(cb), "+s"(vcu_), "+s"(wave_))
; __device__ __forceinline__ void xcd_barrier(const XcdBarrier& b, const bool group_local = false, const bool xcc_only = false) {
;     asm volatile("s_waitcnt vmcnt(0)" ::: "memory");
;     __syncthreads();
;     if (threadIdx.x == 0) {
;         GAS unsigned* barg = (GAS unsigned*)b.bar; asm volatile("" : "+s"(barg)); unsigned* bar = (unsigned*)barg;
;         __builtin_amdgcn_s_waitcnt(0);
;         unsigned nloc = b.st[0], nx = b.st[1];
;         if (nloc == 0u) { xcd_barrier_complete(bar, b.x, nloc, nx); b.st[0] = nloc; b.st[1] = nx; }
;         const unsigned old = xb_add(&bar[XB_XSUB(b.x)], 1u);
; __global__ void __launch_bounds__(NWAVES * 64, 2) mk_fwd(Args args) {
;     ...
;         if (IN(pb + 4)) { TSTART();
;             WSL(); const bf16* WL = (const bf16*)(wl + WS_W) + (size_t)l * LAYER_W_ELEMS;
;             pg8::Gemm g{(const bf16*)(wl + WS_XR), WL + W_GU, MTOK, 2 * DFF, DM};
;     ...
;             if (PROBE_KIND != 24 && PROBE_KIND != 26 && PROBE_KIND != 27 && PROBE_KIND != 28) g.probe = (unsigned*)(wl + WS_CTL) + 3008;
;     ...
;             pg8::StaticOrder S; S.init(MTOK, 2 * DFF, F.G, cb);
.LBB0_1358:
	v_readlane_b32 s0, v255, 23
	s_add_i32 s22, s0, 5
	v_readlane_b32 s0, v255, 6
	v_readlane_b32 s1, v255, 7
	s_cmp_ge_i32 s22, s1
	s_cbranch_scc1 .LBB0_1434
	s_waitcnt vmcnt(0)
	s_waitcnt vmcnt(0) lgkmcnt(0)
	s_barrier
	v_cmp_lt_u32_e32 vcc, 63, v0
	s_and_saveexec_b64 s[14:15], vcc
	s_cbranch_execz .Lwp_gu
	v_readlane_b32 s0, v255, 4
	v_readlane_b32 s1, v255, 5
	v_readlane_b32 s4, v255, 52
	v_readlane_b32 s5, v255, 2
	s_cmp_eq_u32 s4, 3
	s_cbranch_scc1 .Lwp_gu
	s_mul_i32 s4, s4, 0x1dc0000
	s_add_u32 s0, s0, s4
	s_addc_u32 s1, s1, 0
	s_add_u32 s0, s0, 0x1500000
	s_addc_u32 s1, s1, 0
	s_lshr_b32 s5, s5, 3
	s_mul_i32 s5, s5, 448
	v_add_u32_e32 v241, s5, v0
	v_subrev_u32_e32 v241, 64, v241
	v_lshrrev_b32_e32 v242, 1, v241
	v_cmp_gt_u32_e32 vcc, 0x1600, v242
	s_and_b64 exec, exec, vcc
	s_cbranch_execz .Lwp_gu
	v_and_b32_e32 v241, 1, v241
	v_mul_u32_u24_e32 v242, 0x800, v242
	v_lshl_add_u32 v241, v241, 7, v242
	global_load_dword v240, v241, s[0:1]

;     __device__ void init(int M, int N, int G_, int c_) { base.init(M, N, G_, c_); full = base.nwg / G_; split = (base.nwg % G_) * 2 == G_ && (G_ % 16) == 0; }
;     __device__ void init(int G_, int c_) { base.init(MTOK, DM, G_, c_); }
; #define GAS __attribute__((address_space(1)))
; __device__ __forceinline__ unsigned xb_add(unsigned* p, unsigned v) { return __hip_atomic_fetch_add(p, v, __ATOMIC_RELAXED, __HIP_MEMORY_SCOPE_AGENT); }
; #define TSTART() do { tph0 = rt(); } while (0)
; #define TSTART() do {} while (0)
; #define WSL() GAS unsigned char* wlg = (GAS unsigned char*)ws; asm volatile("" : "+s"(wlg)); unsigned char* wl = (unsigned char*)wlg; int cb = (int)blockIdx.x, vcu_ = F.vcu, wave_ = F.wave; asm volatile("" : "+s"(cb), "+s"(vcu_), "+s"(wave_))
; __device__ __forceinline__ void xcd_barrier(const XcdBarrier& b, const bool group_local = false, const bool xcc_only = false) {
;     asm volatile("s_waitcnt vmcnt(0)" ::: "memory");
;     __syncthreads();
;     if (threadIdx.x == 0) {
;         GAS unsigned* barg = (GAS unsigned*)b.bar; asm volatile("" : "+s"(barg)); unsigned* bar = (unsigned*)barg;
;         __builtin_amdgcn_s_waitcnt(0);
;         unsigned nloc = b.st[0], nx = b.st[1];
;         if (nloc == 0u) { xcd_barrier_complete(bar, b.x, nloc, nx); b.st[0] = nloc; b.st[1] = nx; }
;         const unsigned old = xb_add(&bar[XB_XSUB(b.x)], 1u);
; __global__ void __launch_bounds__(NWAVES * 64, 2) mk_fwd(Args args) {
;     ...
;         if (IN(pb + 5)) { TSTART();
;             WSL(); const bf16* WL = (const bf16*)(wl + WS_W) + (size_t)l * LAYER_W_ELEMS;
;             const int pm_cu = 8 * (cb & 7) + ((cb >> 3) & 7);
;             pg8::Gemm g{(const bf16*)(wl + h_panel_off(pm_cu)) - (size_t)pm_cu * 256 * DFF, WL + W_DN, MTOK, DM, DFF}; pg8::StaticOrder S; S.init(MTOK, DM, F.G, cb);
.LBB0_1672:
	v_readlane_b32 s0, v255, 23
	s_add_i32 s22, s0, 6
	v_readlane_b32 s0, v255, 6
	v_readlane_b32 s1, v255, 7
	s_cmp_ge_i32 s22, s1
	s_cbranch_scc1 .LBB0_1748
	s_waitcnt vmcnt(0)
	s_waitcnt vmcnt(0) lgkmcnt(0)
	s_barrier
	v_cmp_lt_u32_e32 vcc, 63, v0
	s_and_saveexec_b64 s[14:15], vcc
	s_cbranch_execz .Lwp_dn
	v_readlane_b32 s0, v255, 4
	v_readlane_b32 s1, v255, 5
	v_readlane_b32 s4, v255, 52
	v_readlane_b32 s5, v255, 2
	s_mul_i32 s4, s4, 0x1dc0000
	s_add_u32 s0, s0, s4
	s_addc_u32 s1, s1, 0
	s_add_u32 s0, s0, 0x2000000
	s_addc_u32 s1, s1, 0
	s_lshr_b32 s5, s5, 3
	s_mul_i32 s5, s5, 448
	v_add_u32_e32 v241, s5, v0
	v_subrev_u32_e32 v241, 64, v241
	v_lshrrev_b32_e32 v242, 3, v241
	v_cmp_gt_u32_e32 vcc, 0x400, v242
	s_and_b64 exec, exec, vcc
	s_cbranch_execz .Lwp_dn
	v_and_b32_e32 v241, 7, v241
	v_mul_u32_u24_e32 v242, 0x1600, v242
	v_lshl_add_u32 v241, v241, 7, v242
	global_load_dword v240, v241, s[0:1]
